# grid barrier polls: longer s_sleep between polls (1 -> 3) to cut poll traffic beside still-running workgroups
# speedup vs baseline: 1.0040x; 1.0001x over previous
; __device__ __forceinline__ unsigned xb_ld(unsigned* p)              { return __hip_atomic_load(p, __ATOMIC_RELAXED, __HIP_MEMORY_SCOPE_AGENT); }
; __device__ __forceinline__ void xcd_barrier_complete(unsigned* bar, unsigned x, unsigned& nloc, unsigned& nx) {
;     ...
;     for (;;) {
;         sum = 0u; cnt = 0u; mine = 0u;
; #pragma unroll
;         for (unsigned j = 0; j < 16; ++j) { const unsigned c = xb_ld(&bar[XB_XCNT(j)]); sum += c; cnt += (c > 0u) ? 1u : 0u; mine = (j == x) ? c : mine; }
;         if (sum == G) break;
;         __builtin_amdgcn_s_sleep(1);
;         if ((++sp & 255u) == 0u) { if (xb_ld(&bar[XB_TMO])) break; if (sp > XB_SPIN_CAP) { atomicAdd(&bar[XB_TMO], 1u); break; } }
;     }
.LBB0_82:
	global_load_dword v15, v16, s[8:9] sc1
	global_load_dword v0, v16, s[10:11] sc1
	global_load_dword v1, v16, s[16:17] sc1
	global_load_dword v2, v16, s[18:19] sc1
	global_load_dword v3, v16, s[20:21] sc1
	global_load_dword v4, v16, s[22:23] sc1
	global_load_dword v5, v16, s[24:25] sc1
	global_load_dword v6, v16, s[26:27] sc1
	global_load_dword v7, v16, s[28:29] sc1
	global_load_dword v8, v16, s[30:31] sc1
	global_load_dword v9, v16, s[34:35] sc1
	global_load_dword v10, v16, s[36:37] sc1
	global_load_dword v11, v16, s[38:39] sc1
	global_load_dword v12, v16, s[40:41] sc1
	global_load_dword v13, v16, s[42:43] sc1
	global_load_dword v14, v16, s[44:45] sc1
	s_mov_b64 s[46:47], -1
	s_mov_b64 s[48:49], -1
	s_waitcnt vmcnt(14)
	v_add_u32_e32 v17, v0, v15
	s_waitcnt vmcnt(13)
	v_add_u32_e32 v17, v17, v1
	s_waitcnt vmcnt(12)
	v_add_u32_e32 v17, v17, v2
	s_waitcnt vmcnt(11)
	v_add_u32_e32 v17, v17, v3
	s_waitcnt vmcnt(10)
	v_add_u32_e32 v17, v17, v4
	s_waitcnt vmcnt(9)
	v_add_u32_e32 v17, v17, v5
	s_waitcnt vmcnt(8)
	v_add_u32_e32 v17, v17, v6
	s_waitcnt vmcnt(7)
	v_add_u32_e32 v17, v17, v7
	s_waitcnt vmcnt(6)
	v_add_u32_e32 v17, v17, v8
	s_waitcnt vmcnt(5)
	v_add_u32_e32 v17, v17, v9
	s_waitcnt vmcnt(4)
	v_add_u32_e32 v17, v17, v10
	s_waitcnt vmcnt(3)
	v_add_u32_e32 v17, v17, v11
	s_waitcnt vmcnt(2)
	v_add_u32_e32 v17, v17, v12
	s_waitcnt vmcnt(1)
	v_add_u32_e32 v17, v17, v13
	s_waitcnt vmcnt(0)
	v_add_u32_e32 v17, v17, v14
	v_cmp_eq_u32_e32 vcc, s13, v17
	s_cbranch_vccnz .LBB0_81
	s_and_b32 s33, s15, 0xff
	s_cmp_eq_u32 s33, 0
	s_mov_b64 s[50:51], -1
	s_sleep 3
	s_cbranch_scc1 .LBB0_86
	s_and_b64 vcc, exec, s[50:51]
	s_cbranch_vccz .LBB0_80

.LBB0_98:
	s_and_b32 s15, s13, 0xff
	s_mov_b64 s[24:25], -1
	s_cmp_lg_u32 s15, 0
	s_mov_b64 s[28:29], -1
	s_sleep 3
	s_cbranch_scc0 .LBB0_101
	s_and_b64 vcc, exec, s[28:29]
	s_cbranch_vccz .LBB0_97

.LBB0_115:
	s_and_b32 s15, s13, 0xff
	s_cmp_lg_u32 s15, 0
	s_mov_b64 s[26:27], -1
	s_sleep 3
	s_cbranch_scc0 .LBB0_118
	s_mov_b64 s[28:29], -1
	s_and_b64 vcc, exec, s[26:27]
	s_cbranch_vccz .LBB0_114

; __device__ __forceinline__ unsigned xb_ld(unsigned* p)              { return __hip_atomic_load(p, __ATOMIC_RELAXED, __HIP_MEMORY_SCOPE_AGENT); }
; __device__ __forceinline__ void xcd_barrier_complete(unsigned* bar, unsigned x, unsigned& nloc, unsigned& nx) {
;     ...
;     for (;;) {
;         sum = 0u; cnt = 0u; mine = 0u;
; #pragma unroll
;         for (unsigned j = 0; j < 16; ++j) { const unsigned c = xb_ld(&bar[XB_XCNT(j)]); sum += c; cnt += (c > 0u) ? 1u : 0u; mine = (j == x) ? c : mine; }
;         if (sum == G) break;
;         __builtin_amdgcn_s_sleep(1);
;         if ((++sp & 255u) == 0u) { if (xb_ld(&bar[XB_TMO])) break; if (sp > XB_SPIN_CAP) { atomicAdd(&bar[XB_TMO], 1u); break; } }
;     }
.LBB0_143:
	global_load_dword v15, v16, s[6:7] sc1
	global_load_dword v0, v16, s[8:9] sc1
	global_load_dword v1, v16, s[10:11] sc1
	global_load_dword v2, v16, s[16:17] sc1
	global_load_dword v3, v16, s[18:19] sc1
	global_load_dword v4, v16, s[20:21] sc1
	global_load_dword v5, v16, s[22:23] sc1
	global_load_dword v6, v16, s[24:25] sc1
	global_load_dword v7, v16, s[26:27] sc1
	global_load_dword v8, v16, s[28:29] sc1
	global_load_dword v9, v16, s[30:31] sc1
	global_load_dword v10, v16, s[34:35] sc1
	global_load_dword v11, v16, s[36:37] sc1
	global_load_dword v12, v16, s[38:39] sc1
	global_load_dword v13, v16, s[40:41] sc1
	global_load_dword v14, v16, s[42:43] sc1
	s_mov_b64 s[44:45], -1
	s_mov_b64 s[46:47], -1
	s_waitcnt vmcnt(14)
	v_add_u32_e32 v17, v0, v15
	s_waitcnt vmcnt(13)
	v_add_u32_e32 v17, v17, v1
	s_waitcnt vmcnt(12)
	v_add_u32_e32 v17, v17, v2
	s_waitcnt vmcnt(11)
	v_add_u32_e32 v17, v17, v3
	s_waitcnt vmcnt(10)
	v_add_u32_e32 v17, v17, v4
	s_waitcnt vmcnt(9)
	v_add_u32_e32 v17, v17, v5
	s_waitcnt vmcnt(8)
	v_add_u32_e32 v17, v17, v6
	s_waitcnt vmcnt(7)
	v_add_u32_e32 v17, v17, v7
	s_waitcnt vmcnt(6)
	v_add_u32_e32 v17, v17, v8
	s_waitcnt vmcnt(5)
	v_add_u32_e32 v17, v17, v9
	s_waitcnt vmcnt(4)
	v_add_u32_e32 v17, v17, v10
	s_waitcnt vmcnt(3)
	v_add_u32_e32 v17, v17, v11
	s_waitcnt vmcnt(2)
	v_add_u32_e32 v17, v17, v12
	s_waitcnt vmcnt(1)
	v_add_u32_e32 v17, v17, v13
	s_waitcnt vmcnt(0)
	v_add_u32_e32 v17, v17, v14
	v_cmp_eq_u32_e32 vcc, s13, v17
	s_cbranch_vccnz .LBB0_142
	s_and_b32 s33, s15, 0xff
	s_cmp_eq_u32 s33, 0
	s_mov_b64 s[48:49], -1
	s_sleep 3
	s_cbranch_scc1 .LBB0_147
	s_and_b64 vcc, exec, s[48:49]
	s_cbranch_vccz .LBB0_141

.LBB0_159:
	s_and_b32 s15, s13, 0xff
	s_mov_b64 s[22:23], -1
	s_cmp_lg_u32 s15, 0
	s_mov_b64 s[26:27], -1
	s_sleep 3
	s_cbranch_scc0 .LBB0_162
	s_and_b64 vcc, exec, s[26:27]
	s_cbranch_vccz .LBB0_158

.LBB0_176:
	s_and_b32 s15, s13, 0xff
	s_cmp_lg_u32 s15, 0
	s_mov_b64 s[24:25], -1
	s_sleep 3
	s_cbranch_scc0 .LBB0_179
	s_mov_b64 s[26:27], -1
	s_and_b64 vcc, exec, s[24:25]
	s_cbranch_vccz .LBB0_175

; __device__ __forceinline__ unsigned xb_ld(unsigned* p)              { return __hip_atomic_load(p, __ATOMIC_RELAXED, __HIP_MEMORY_SCOPE_AGENT); }
; __device__ __forceinline__ void xcd_barrier_complete(unsigned* bar, unsigned x, unsigned& nloc, unsigned& nx) {
;     ...
;     for (;;) {
;         sum = 0u; cnt = 0u; mine = 0u;
; #pragma unroll
;         for (unsigned j = 0; j < 16; ++j) { const unsigned c = xb_ld(&bar[XB_XCNT(j)]); sum += c; cnt += (c > 0u) ? 1u : 0u; mine = (j == x) ? c : mine; }
;         if (sum == G) break;
;         __builtin_amdgcn_s_sleep(1);
;         if ((++sp & 255u) == 0u) { if (xb_ld(&bar[XB_TMO])) break; if (sp > XB_SPIN_CAP) { atomicAdd(&bar[XB_TMO], 1u); break; } }
;     }
.LBB0_217:
	v_readlane_b32 s0, v246, 55
	v_readlane_b32 s1, v246, 56
	s_mov_b64 s[10:11], -1
	s_nop 3
	global_load_dword v0, v153, s[0:1] sc1
	v_readlane_b32 s0, v246, 57
	v_readlane_b32 s1, v246, 58
	s_nop 4
	global_load_dword v1, v153, s[0:1] sc1
	v_readlane_b32 s0, v246, 59
	v_readlane_b32 s1, v246, 60
	s_waitcnt vmcnt(0)
	v_add_u32_e32 v16, v1, v0
	s_nop 2
	global_load_dword v2, v153, s[0:1] sc1
	v_readlane_b32 s0, v246, 61
	v_readlane_b32 s1, v246, 62
	s_waitcnt vmcnt(0)
	v_add_u32_e32 v16, v16, v2
	s_nop 2
	global_load_dword v3, v153, s[0:1] sc1
	v_readlane_b32 s0, v246, 63
	v_readlane_b32 s1, v247, 0
	s_waitcnt vmcnt(0)
	v_add_u32_e32 v16, v16, v3
	s_nop 2
	global_load_dword v4, v153, s[0:1] sc1
	v_readlane_b32 s0, v247, 1
	v_readlane_b32 s1, v247, 2
	s_waitcnt vmcnt(0)
	v_add_u32_e32 v16, v16, v4
	s_nop 2
	global_load_dword v5, v153, s[0:1] sc1
	v_readlane_b32 s0, v247, 3
	v_readlane_b32 s1, v247, 4
	s_waitcnt vmcnt(0)
	v_add_u32_e32 v16, v16, v5
	s_nop 2
	global_load_dword v6, v153, s[0:1] sc1
	v_readlane_b32 s0, v247, 5
	v_readlane_b32 s1, v247, 6
	s_waitcnt vmcnt(0)
	v_add_u32_e32 v16, v16, v6
	s_nop 2
	global_load_dword v7, v153, s[0:1] sc1
	v_readlane_b32 s0, v247, 7
	v_readlane_b32 s1, v247, 8
	s_waitcnt vmcnt(0)
	v_add_u32_e32 v16, v16, v7
	s_nop 2
	global_load_dword v8, v153, s[0:1] sc1
	v_readlane_b32 s0, v247, 9
	v_readlane_b32 s1, v247, 10
	s_waitcnt vmcnt(0)
	v_add_u32_e32 v16, v16, v8
	s_nop 2
	global_load_dword v9, v153, s[0:1] sc1
	v_readlane_b32 s0, v247, 11
	v_readlane_b32 s1, v247, 12
	s_waitcnt vmcnt(0)
	v_add_u32_e32 v16, v16, v9
	s_nop 2
	global_load_dword v10, v153, s[0:1] sc1
	v_readlane_b32 s0, v247, 13
	v_readlane_b32 s1, v247, 14
	s_waitcnt vmcnt(0)
	v_add_u32_e32 v16, v16, v10
	s_nop 2
	global_load_dword v11, v153, s[0:1] sc1
	v_readlane_b32 s0, v247, 15
	v_readlane_b32 s1, v247, 16
	s_waitcnt vmcnt(0)
	v_add_u32_e32 v16, v16, v11
	s_nop 2
	global_load_dword v12, v153, s[0:1] sc1
	v_readlane_b32 s0, v247, 17
	v_readlane_b32 s1, v247, 18
	s_waitcnt vmcnt(0)
	v_add_u32_e32 v16, v16, v12
	s_nop 2
	global_load_dword v13, v153, s[0:1] sc1
	v_readlane_b32 s0, v247, 19
	v_readlane_b32 s1, v247, 20
	s_waitcnt vmcnt(0)
	v_add_u32_e32 v16, v16, v13
	s_nop 2
	global_load_dword v14, v153, s[0:1] sc1
	v_readlane_b32 s0, v247, 21
	v_readlane_b32 s1, v247, 22
	s_waitcnt vmcnt(0)
	v_add_u32_e32 v16, v16, v14
	s_nop 2
	global_load_dword v15, v153, s[0:1] sc1
	s_mov_b64 s[0:1], -1
	s_waitcnt vmcnt(0)
	v_add_u32_e32 v16, v16, v15
	v_cmp_eq_u32_e32 vcc, s14, v16
	s_cbranch_vccnz .LBB0_216
	s_and_b32 s0, s15, 0xff
	s_cmp_eq_u32 s0, 0
	s_mov_b64 s[0:1], -1
	s_mov_b64 s[12:13], -1
	s_sleep 3
	s_cbranch_scc1 .LBB0_221
	s_and_b64 vcc, exec, s[12:13]
	s_cbranch_vccz .LBB0_216

.LBB0_233:
	s_and_b32 s2, s31, 0xff
	s_mov_b64 s[16:17], -1
	s_cmp_lg_u32 s2, 0
	s_mov_b64 s[40:41], -1
	s_sleep 3
	s_cbranch_scc0 .LBB0_236
	s_and_b64 vcc, exec, s[40:41]
	s_cbranch_vccz .LBB0_232

.LBB0_386:
	s_and_b32 s2, s40, 0xff
	s_mov_b64 s[16:17], -1
	s_cmp_lg_u32 s2, 0
	s_mov_b64 s[42:43], -1
	s_sleep 3
	s_cbranch_scc0 .LBB0_389
	s_and_b64 vcc, exec, s[42:43]
	s_cbranch_vccz .LBB0_385

; __device__ __forceinline__ unsigned xb_ld(unsigned* p)              { return __hip_atomic_load(p, __ATOMIC_RELAXED, __HIP_MEMORY_SCOPE_AGENT); }
; __device__ __forceinline__ void xcd_barrier_complete(unsigned* bar, unsigned x, unsigned& nloc, unsigned& nx) {
;     ...
;     for (;;) {
;         sum = 0u; cnt = 0u; mine = 0u;
; #pragma unroll
;         for (unsigned j = 0; j < 16; ++j) { const unsigned c = xb_ld(&bar[XB_XCNT(j)]); sum += c; cnt += (c > 0u) ? 1u : 0u; mine = (j == x) ? c : mine; }
;         if (sum == G) break;
;         __builtin_amdgcn_s_sleep(1);
;         if ((++sp & 255u) == 0u) { if (xb_ld(&bar[XB_TMO])) break; if (sp > XB_SPIN_CAP) { atomicAdd(&bar[XB_TMO], 1u); break; } }
;     }
.LBB0_778:
	v_readlane_b32 s0, v246, 55
	v_readlane_b32 s1, v246, 56
	s_mov_b64 s[10:11], -1
	s_nop 3
	global_load_dword v0, v153, s[0:1] sc1
	v_readlane_b32 s0, v246, 57
	v_readlane_b32 s1, v246, 58
	s_nop 4
	global_load_dword v1, v153, s[0:1] sc1
	v_readlane_b32 s0, v246, 59
	v_readlane_b32 s1, v246, 60
	s_waitcnt vmcnt(0)
	v_add_u32_e32 v16, v1, v0
	s_nop 2
	global_load_dword v2, v153, s[0:1] sc1
	v_readlane_b32 s0, v246, 61
	v_readlane_b32 s1, v246, 62
	s_waitcnt vmcnt(0)
	v_add_u32_e32 v16, v16, v2
	s_nop 2
	global_load_dword v3, v153, s[0:1] sc1
	v_readlane_b32 s0, v246, 63
	v_readlane_b32 s1, v247, 0
	s_waitcnt vmcnt(0)
	v_add_u32_e32 v16, v16, v3
	s_nop 2
	global_load_dword v4, v153, s[0:1] sc1
	v_readlane_b32 s0, v247, 1
	v_readlane_b32 s1, v247, 2
	s_waitcnt vmcnt(0)
	v_add_u32_e32 v16, v16, v4
	s_nop 2
	global_load_dword v5, v153, s[0:1] sc1
	v_readlane_b32 s0, v247, 3
	v_readlane_b32 s1, v247, 4
	s_waitcnt vmcnt(0)
	v_add_u32_e32 v16, v16, v5
	s_nop 2
	global_load_dword v6, v153, s[0:1] sc1
	v_readlane_b32 s0, v247, 5
	v_readlane_b32 s1, v247, 6
	s_waitcnt vmcnt(0)
	v_add_u32_e32 v16, v16, v6
	s_nop 2
	global_load_dword v7, v153, s[0:1] sc1
	v_readlane_b32 s0, v247, 7
	v_readlane_b32 s1, v247, 8
	s_waitcnt vmcnt(0)
	v_add_u32_e32 v16, v16, v7
	s_nop 2
	global_load_dword v8, v153, s[0:1] sc1
	v_readlane_b32 s0, v247, 9
	v_readlane_b32 s1, v247, 10
	s_waitcnt vmcnt(0)
	v_add_u32_e32 v16, v16, v8
	s_nop 2
	global_load_dword v9, v153, s[0:1] sc1
	v_readlane_b32 s0, v247, 11
	v_readlane_b32 s1, v247, 12
	s_waitcnt vmcnt(0)
	v_add_u32_e32 v16, v16, v9
	s_nop 2
	global_load_dword v10, v153, s[0:1] sc1
	v_readlane_b32 s0, v247, 13
	v_readlane_b32 s1, v247, 14
	s_waitcnt vmcnt(0)
	v_add_u32_e32 v16, v16, v10
	s_nop 2
	global_load_dword v11, v153, s[0:1] sc1
	v_readlane_b32 s0, v247, 15
	v_readlane_b32 s1, v247, 16
	s_waitcnt vmcnt(0)
	v_add_u32_e32 v16, v16, v11
	s_nop 2
	global_load_dword v12, v153, s[0:1] sc1
	v_readlane_b32 s0, v247, 17
	v_readlane_b32 s1, v247, 18
	s_waitcnt vmcnt(0)
	v_add_u32_e32 v16, v16, v12
	s_nop 2
	global_load_dword v13, v153, s[0:1] sc1
	v_readlane_b32 s0, v247, 19
	v_readlane_b32 s1, v247, 20
	s_waitcnt vmcnt(0)
	v_add_u32_e32 v16, v16, v13
	s_nop 2
	global_load_dword v14, v153, s[0:1] sc1
	v_readlane_b32 s0, v247, 21
	v_readlane_b32 s1, v247, 22
	s_waitcnt vmcnt(0)
	v_add_u32_e32 v16, v16, v14
	s_nop 2
	global_load_dword v15, v153, s[0:1] sc1
	s_mov_b64 s[0:1], -1
	s_waitcnt vmcnt(0)
	v_add_u32_e32 v16, v16, v15
	v_cmp_eq_u32_e32 vcc, s5, v16
	s_cbranch_vccnz .LBB0_777
	s_and_b32 s0, s14, 0xff
	s_cmp_eq_u32 s0, 0
	s_mov_b64 s[0:1], -1
	s_mov_b64 s[12:13], -1
	s_sleep 3
	s_cbranch_scc1 .LBB0_782
	s_and_b64 vcc, exec, s[12:13]
	s_cbranch_vccz .LBB0_777

.LBB0_794:
	s_and_b32 s2, s5, 0xff
	s_mov_b64 s[16:17], -1
	s_cmp_lg_u32 s2, 0
	s_mov_b64 s[40:41], -1
	s_sleep 3
	s_cbranch_scc0 .LBB0_797
	s_and_b64 vcc, exec, s[40:41]
	s_cbranch_vccz .LBB0_793

; __device__ __forceinline__ unsigned xb_ld(unsigned* p)              { return __hip_atomic_load(p, __ATOMIC_RELAXED, __HIP_MEMORY_SCOPE_AGENT); }
; __device__ __forceinline__ void xcd_barrier_complete(unsigned* bar, unsigned x, unsigned& nloc, unsigned& nx) {
;     ...
;     for (;;) {
;         sum = 0u; cnt = 0u; mine = 0u;
; #pragma unroll
;         for (unsigned j = 0; j < 16; ++j) { const unsigned c = xb_ld(&bar[XB_XCNT(j)]); sum += c; cnt += (c > 0u) ? 1u : 0u; mine = (j == x) ? c : mine; }
;         if (sum == G) break;
;         __builtin_amdgcn_s_sleep(1);
;         if ((++sp & 255u) == 0u) { if (xb_ld(&bar[XB_TMO])) break; if (sp > XB_SPIN_CAP) { atomicAdd(&bar[XB_TMO], 1u); break; } }
;     }
.LBB0_1095:
	v_readlane_b32 s0, v246, 55
	v_readlane_b32 s1, v246, 56
	s_mov_b64 s[8:9], -1
	s_nop 3
	global_load_dword v0, v153, s[0:1] sc1
	v_readlane_b32 s0, v246, 57
	v_readlane_b32 s1, v246, 58
	s_nop 4
	global_load_dword v1, v153, s[0:1] sc1
	v_readlane_b32 s0, v246, 59
	v_readlane_b32 s1, v246, 60
	s_waitcnt vmcnt(0)
	v_add_u32_e32 v16, v1, v0
	s_nop 2
	global_load_dword v2, v153, s[0:1] sc1
	v_readlane_b32 s0, v246, 61
	v_readlane_b32 s1, v246, 62
	s_waitcnt vmcnt(0)
	v_add_u32_e32 v16, v16, v2
	s_nop 2
	global_load_dword v3, v153, s[0:1] sc1
	v_readlane_b32 s0, v246, 63
	v_readlane_b32 s1, v247, 0
	s_waitcnt vmcnt(0)
	v_add_u32_e32 v16, v16, v3
	s_nop 2
	global_load_dword v4, v153, s[0:1] sc1
	v_readlane_b32 s0, v247, 1
	v_readlane_b32 s1, v247, 2
	s_waitcnt vmcnt(0)
	v_add_u32_e32 v16, v16, v4
	s_nop 2
	global_load_dword v5, v153, s[0:1] sc1
	v_readlane_b32 s0, v247, 3
	v_readlane_b32 s1, v247, 4
	s_waitcnt vmcnt(0)
	v_add_u32_e32 v16, v16, v5
	s_nop 2
	global_load_dword v6, v153, s[0:1] sc1
	v_readlane_b32 s0, v247, 5
	v_readlane_b32 s1, v247, 6
	s_waitcnt vmcnt(0)
	v_add_u32_e32 v16, v16, v6
	s_nop 2
	global_load_dword v7, v153, s[0:1] sc1
	v_readlane_b32 s0, v247, 7
	v_readlane_b32 s1, v247, 8
	s_waitcnt vmcnt(0)
	v_add_u32_e32 v16, v16, v7
	s_nop 2
	global_load_dword v8, v153, s[0:1] sc1
	v_readlane_b32 s0, v247, 9
	v_readlane_b32 s1, v247, 10
	s_waitcnt vmcnt(0)
	v_add_u32_e32 v16, v16, v8
	s_nop 2
	global_load_dword v9, v153, s[0:1] sc1
	v_readlane_b32 s0, v247, 11
	v_readlane_b32 s1, v247, 12
	s_waitcnt vmcnt(0)
	v_add_u32_e32 v16, v16, v9
	s_nop 2
	global_load_dword v10, v153, s[0:1] sc1
	v_readlane_b32 s0, v247, 13
	v_readlane_b32 s1, v247, 14
	s_waitcnt vmcnt(0)
	v_add_u32_e32 v16, v16, v10
	s_nop 2
	global_load_dword v11, v153, s[0:1] sc1
	v_readlane_b32 s0, v247, 15
	v_readlane_b32 s1, v247, 16
	s_waitcnt vmcnt(0)
	v_add_u32_e32 v16, v16, v11
	s_nop 2
	global_load_dword v12, v153, s[0:1] sc1
	v_readlane_b32 s0, v247, 17
	v_readlane_b32 s1, v247, 18
	s_waitcnt vmcnt(0)
	v_add_u32_e32 v16, v16, v12
	s_nop 2
	global_load_dword v13, v153, s[0:1] sc1
	v_readlane_b32 s0, v247, 19
	v_readlane_b32 s1, v247, 20
	s_waitcnt vmcnt(0)
	v_add_u32_e32 v16, v16, v13
	s_nop 2
	global_load_dword v14, v153, s[0:1] sc1
	v_readlane_b32 s0, v247, 21
	v_readlane_b32 s1, v247, 22
	s_waitcnt vmcnt(0)
	v_add_u32_e32 v16, v16, v14
	s_nop 2
	global_load_dword v15, v153, s[0:1] sc1
	s_mov_b64 s[0:1], -1
	s_waitcnt vmcnt(0)
	v_add_u32_e32 v16, v16, v15
	v_cmp_eq_u32_e32 vcc, s12, v16
	s_cbranch_vccnz .LBB0_1094
	s_and_b32 s0, s13, 0xff
	s_cmp_eq_u32 s0, 0
	s_mov_b64 s[0:1], -1
	s_mov_b64 s[10:11], -1
	s_sleep 3
	s_cbranch_scc1 .LBB0_1099
	s_and_b64 vcc, exec, s[10:11]
	s_cbranch_vccz .LBB0_1094

.LBB0_1114:
	s_and_b32 s2, s41, 0xff
	s_mov_b64 s[14:15], -1
	s_cmp_lg_u32 s2, 0
	s_mov_b64 s[18:19], -1
	s_sleep 3
	s_cbranch_scc0 .LBB0_1117
	s_and_b64 vcc, exec, s[18:19]
	s_cbranch_vccz .LBB0_1113

.LBB0_1332:
	s_and_b32 s2, s43, 0xff
	s_mov_b64 s[16:17], -1
	s_cmp_lg_u32 s2, 0
	s_mov_b64 s[40:41], -1
	s_sleep 3
	s_cbranch_scc0 .LBB0_1335
	s_and_b64 vcc, exec, s[40:41]
	s_cbranch_vccz .LBB0_1331

; __device__ __forceinline__ unsigned xb_ld(unsigned* p)              { return __hip_atomic_load(p, __ATOMIC_RELAXED, __HIP_MEMORY_SCOPE_AGENT); }
; __device__ __forceinline__ void xcd_barrier_complete(unsigned* bar, unsigned x, unsigned& nloc, unsigned& nx) {
;     ...
;     for (;;) {
;         sum = 0u; cnt = 0u; mine = 0u;
; #pragma unroll
;         for (unsigned j = 0; j < 16; ++j) { const unsigned c = xb_ld(&bar[XB_XCNT(j)]); sum += c; cnt += (c > 0u) ? 1u : 0u; mine = (j == x) ? c : mine; }
;         if (sum == G) break;
;         __builtin_amdgcn_s_sleep(1);
;         if ((++sp & 255u) == 0u) { if (xb_ld(&bar[XB_TMO])) break; if (sp > XB_SPIN_CAP) { atomicAdd(&bar[XB_TMO], 1u); break; } }
;     }
.LBB0_1695:
	v_readlane_b32 s0, v246, 55
	v_readlane_b32 s1, v246, 56
	s_mov_b64 s[8:9], -1
	s_nop 3
	global_load_dword v0, v153, s[0:1] sc1
	v_readlane_b32 s0, v246, 57
	v_readlane_b32 s1, v246, 58
	s_nop 4
	global_load_dword v1, v153, s[0:1] sc1
	v_readlane_b32 s0, v246, 59
	v_readlane_b32 s1, v246, 60
	s_waitcnt vmcnt(0)
	v_add_u32_e32 v16, v1, v0
	s_nop 2
	global_load_dword v2, v153, s[0:1] sc1
	v_readlane_b32 s0, v246, 61
	v_readlane_b32 s1, v246, 62
	s_waitcnt vmcnt(0)
	v_add_u32_e32 v16, v16, v2
	s_nop 2
	global_load_dword v3, v153, s[0:1] sc1
	v_readlane_b32 s0, v246, 63
	v_readlane_b32 s1, v247, 0
	s_waitcnt vmcnt(0)
	v_add_u32_e32 v16, v16, v3
	s_nop 2
	global_load_dword v4, v153, s[0:1] sc1
	v_readlane_b32 s0, v247, 1
	v_readlane_b32 s1, v247, 2
	s_waitcnt vmcnt(0)
	v_add_u32_e32 v16, v16, v4
	s_nop 2
	global_load_dword v5, v153, s[0:1] sc1
	v_readlane_b32 s0, v247, 3
	v_readlane_b32 s1, v247, 4
	s_waitcnt vmcnt(0)
	v_add_u32_e32 v16, v16, v5
	s_nop 2
	global_load_dword v6, v153, s[0:1] sc1
	v_readlane_b32 s0, v247, 5
	v_readlane_b32 s1, v247, 6
	s_waitcnt vmcnt(0)
	v_add_u32_e32 v16, v16, v6
	s_nop 2
	global_load_dword v7, v153, s[0:1] sc1
	v_readlane_b32 s0, v247, 7
	v_readlane_b32 s1, v247, 8
	s_waitcnt vmcnt(0)
	v_add_u32_e32 v16, v16, v7
	s_nop 2
	global_load_dword v8, v153, s[0:1] sc1
	v_readlane_b32 s0, v247, 9
	v_readlane_b32 s1, v247, 10
	s_waitcnt vmcnt(0)
	v_add_u32_e32 v16, v16, v8
	s_nop 2
	global_load_dword v9, v153, s[0:1] sc1
	v_readlane_b32 s0, v247, 11
	v_readlane_b32 s1, v247, 12
	s_waitcnt vmcnt(0)
	v_add_u32_e32 v16, v16, v9
	s_nop 2
	global_load_dword v10, v153, s[0:1] sc1
	v_readlane_b32 s0, v247, 13
	v_readlane_b32 s1, v247, 14
	s_waitcnt vmcnt(0)
	v_add_u32_e32 v16, v16, v10
	s_nop 2
	global_load_dword v11, v153, s[0:1] sc1
	v_readlane_b32 s0, v247, 15
	v_readlane_b32 s1, v247, 16
	s_waitcnt vmcnt(0)
	v_add_u32_e32 v16, v16, v11
	s_nop 2
	global_load_dword v12, v153, s[0:1] sc1
	v_readlane_b32 s0, v247, 17
	v_readlane_b32 s1, v247, 18
	s_waitcnt vmcnt(0)
	v_add_u32_e32 v16, v16, v12
	s_nop 2
	global_load_dword v13, v153, s[0:1] sc1
	v_readlane_b32 s0, v247, 19
	v_readlane_b32 s1, v247, 20
	s_waitcnt vmcnt(0)
	v_add_u32_e32 v16, v16, v13
	s_nop 2
	global_load_dword v14, v153, s[0:1] sc1
	v_readlane_b32 s0, v247, 21
	v_readlane_b32 s1, v247, 22
	s_waitcnt vmcnt(0)
	v_add_u32_e32 v16, v16, v14
	s_nop 2
	global_load_dword v15, v153, s[0:1] sc1
	s_mov_b64 s[0:1], -1
	s_waitcnt vmcnt(0)
	v_add_u32_e32 v16, v16, v15
	v_cmp_eq_u32_e32 vcc, s5, v16
	s_cbranch_vccnz .LBB0_1694
	s_and_b32 s0, s12, 0xff
	s_cmp_eq_u32 s0, 0
	s_mov_b64 s[0:1], -1
	s_mov_b64 s[10:11], -1
	s_sleep 3
	s_cbranch_scc1 .LBB0_1699
	s_and_b64 vcc, exec, s[10:11]
	s_cbranch_vccz .LBB0_1694

.LBB0_1711:
	s_and_b32 s2, s5, 0xff
	s_mov_b64 s[14:15], -1
	s_cmp_lg_u32 s2, 0
	s_mov_b64 s[18:19], -1
	s_sleep 3
	s_cbranch_scc0 .LBB0_1714
	s_and_b64 vcc, exec, s[18:19]
	s_cbranch_vccz .LBB0_1710
